# speedup vs baseline: 1.0049x; 1.0049x over previous
_Z11attn_kernelPKDF16_S0_S0_PDF16_P15HIP_vector_typeIfLj2EE:
	s_mov_b32 s28, s2
	s_load_dwordx4 s[32:35], s[0:1], 0x8
	v_readfirstlane_b32 s3, v0
	s_ashr_i32 s12, s2, 5
	s_lshr_b32 s21, s3, 6
	s_and_b32 s3, s2, 7
	s_and_b32 s12, s12, -8
	s_load_dwordx8 s[4:11], s[0:1], 0x0
	s_or_b32 s12, s12, s3
	s_bfe_u32 s20, s2, 0x10003
	s_lshl_b32 s2, s2, 3
	s_and_b32 s2, s2, 0x780
	s_lshl_b32 s3, s21, 5
	s_ashr_i32 s13, s12, 31
	s_add_i32 s2, s3, s2
	s_lshl_b64 s[16:17], s[12:13], 11
	s_lshl_b32 s3, s20, 10
	s_or_b32 s14, s16, s3
	s_mov_b32 s15, s17
	s_lshl_b64 s[18:19], s[14:15], 7
	s_lshl_b64 s[14:15], s[12:13], 18
	s_waitcnt lgkmcnt(0)
	s_add_u32 s3, s8, s14
	s_addc_u32 s22, s9, s15
	s_add_u32 s16, s16, s2
	v_and_b32_e32 v98, 31, v0
	s_addc_u32 s17, s17, 0
	v_or_b32_e32 v2, s16, v98
	v_mov_b32_e32 v3, s17
	v_bfe_u32 v54, v0, 5, 1
	v_lshlrev_b64 v[2:3], 7, v[2:3]
	v_mov_b32_e32 v51, 0
	v_lshl_add_u64 v[2:3], s[4:5], 0, v[2:3]
	v_lshlrev_b32_e32 v50, 4, v54
	v_lshl_add_u64 v[2:3], v[2:3], 0, v[50:51]
	s_add_u32 s18, s6, s18
	v_bfe_u32 v1, v0, 3, 3
	s_addc_u32 s19, s7, s19
	s_lshl_b64 s[44:45], s[16:17], 7
	s_add_u32 s44, s4, s44
	s_addc_u32 s45, s5, s45
	v_and_b32_e32 v152, 63, v0
	v_lshlrev_b32_e32 v152, 4, v152
	global_load_dwordx4 v[94:97], v152, s[44:45] nt
	global_load_dwordx4 v[90:93], v152, s[44:45] offset:1024 nt
	global_load_dwordx4 v[86:89], v152, s[44:45] offset:2048 nt
	global_load_dwordx4 v[82:85], v152, s[44:45] offset:3072 nt
	s_lshl_b32 s24, s20, 11
	v_lshl_or_b32 v2, s21, 4, v1
	v_and_b32_e32 v99, 63, v0
	s_add_u32 s4, s3, s24
	v_or_b32_e32 v3, 8, v2
	v_lshlrev_b32_e32 v4, 4, v0
	s_movk_i32 s3, 0x70
	v_bitop3_b32 v53, v99, s3, v4 bitop3:0x48
	v_lshrrev_b32_e32 v4, 1, v3
	v_xor_b32_e32 v4, v4, v0
	s_addc_u32 s5, s22, 0
	v_lshlrev_b32_e32 v4, 4, v4
	s_lshl_b32 s22, s21, 11
	v_and_b32_e32 v52, 0x70, v4
	v_lshl_or_b32 v55, v2, 7, v53
	s_mov_b32 m0, s22
	v_lshl_or_b32 v64, v3, 7, v52
	global_load_lds_dwordx4 v55, s[18:19]
	s_or_b32 m0, s22, 0x400
	v_lshl_or_b32 v50, v2, 12, v53
	global_load_lds_dwordx4 v64, s[18:19]
	s_add_i32 m0, s22, 0x2000
	v_lshl_or_b32 v2, v3, 12, v52
	global_load_lds_dwordx4 v50, s[4:5]
	s_add_i32 m0, s22, 0x2400
	v_mov_b32_e32 v3, v51
	global_load_lds_dwordx4 v2, s[4:5]
	s_add_i32 m0, s22, 0x4000
	v_lshl_add_u64 v[60:61], s[4:5], 0, v[50:51]
	v_lshl_add_u64 v[62:63], s[4:5], 0, v[2:3]
	s_add_u32 s4, s18, 0x2000
	s_addc_u32 s5, s19, 0
	s_add_i32 m0, s22, 0x4400
	s_load_dwordx2 s[0:1], s[0:1], 0x20
	s_mov_b64 s[4:5], 0x80
	v_lshl_add_u64 v[2:3], v[60:61], 0, s[4:5]
	s_add_i32 m0, s22, 0x6000
	v_lshrrev_b32_e32 v4, 1, v0
	v_lshl_add_u64 v[2:3], v[62:63], 0, s[4:5]
	s_add_i32 m0, s22, 0x6400
	v_and_b32_e32 v5, 4, v4
	v_lshlrev_b32_e32 v3, 1, v0
	v_and_b32_e32 v2, 19, v0
	v_and_b32_e32 v3, 8, v3
	v_or3_b32 v2, v3, v2, v5
	s_waitcnt vmcnt(4)
	s_lshl_b32 s46, s21, 12
	s_add_i32 s46, s46, 0x8000
	v_and_b32_e32 v153, 63, v0
	v_lshrrev_b32_e32 v154, 3, v153
	v_lshlrev_b32_e32 v154, 7, v154
	v_lshrrev_b32_e32 v155, 4, v153
	v_xor_b32_e32 v155, v155, v153
	v_and_b32_e32 v155, 7, v155
	v_lshl_add_u32 v154, v155, 4, v154
	v_add_u32_e32 v154, s46, v154
	v_xor_b32_e32 v155, 64, v154
	ds_write_b128 v154, v[94:97]
	ds_write_b128 v155, v[90:93] offset:1024
	ds_write_b128 v154, v[86:89] offset:2048
	ds_write_b128 v155, v[82:85] offset:3072
	v_bfe_u32 v156, v0, 1, 3
	v_xor_b32_e32 v156, v156, v54
	v_lshlrev_b32_e32 v156, 4, v156
	v_lshl_add_u32 v156, v98, 7, v156
	v_add_u32_e32 v156, s46, v156
	v_xor_b32_e32 v157, 32, v156
	v_xor_b32_e32 v158, 64, v156
	v_xor_b32_e32 v159, 0x60, v156
	s_waitcnt lgkmcnt(0)
	ds_read_b128 v[94:97], v156
	ds_read_b128 v[90:93], v157
	ds_read_b128 v[86:89], v158
	ds_read_b128 v[82:85], v159
	s_waitcnt vmcnt(0) lgkmcnt(0)
	v_lshlrev_b32_e32 v115, 7, v2
	v_lshrrev_b32_e32 v3, 1, v2
	v_bfe_u32 v46, v2, 1, 3
	v_bitop3_b32 v2, v54, v4, 7 bitop3:0x78
	s_mov_b32 s3, 0
	v_lshlrev_b32_e32 v108, 3, v54
	s_mov_b32 s23, 1
	s_mov_b64 s[16:17], 0x2000
	v_lshlrev_b32_e32 v109, 7, v98
	v_lshlrev_b32_e32 v110, 4, v2
	s_movk_i32 s25, 0x400
	v_bfe_u32 v50, v0, 1, 3
	s_barrier
	s_and_b32 s29, s28, 7
	s_lshr_b32 s40, s28, 3
	s_lshr_b32 s41, s40, 5
	s_lshl_b32 s41, s41, 3
	s_or_b32 s29, s41, s29
	s_and_b32 s40, s40, 1
	s_lshl_b32 s29, s29, 18
	s_lshl_b32 s41, s40, 17
	s_lshl_b32 s42, s40, 11
	s_add_i32 s41, s41, s29
	s_add_i32 s41, s41, 0x6000
	s_add_i32 s42, s42, s29
	s_add_i32 s42, s42, 0x180
	v_and_b32_e32 v145, 63, v0
	v_lshrrev_b32_e32 v146, 3, v145
	v_lshl_add_u32 v146, s21, 4, v146
	v_and_b32_e32 v145, 7, v145
	v_bfe_u32 v147, v146, 1, 3
	v_xor_b32_e32 v148, v145, v147
	v_xor_b32_e32 v147, 4, v148
	v_lshlrev_b32_e32 v148, 4, v148
	v_lshlrev_b32_e32 v147, 4, v147
	v_lshl_add_u32 v145, v146, 7, v148
	v_lshl_add_u32 v149, v146, 7, v147
	v_add_u32_e32 v149, 0x400, v149
	v_lshl_add_u32 v148, v146, 12, v148
	v_lshl_add_u32 v147, v146, 12, v147
	v_add_u32_e32 v147, 0x8000, v147
	s_waitcnt lgkmcnt(0)
	s_add_u32 s36, s32, s41
	s_addc_u32 s37, s33, 0
	s_add_u32 s38, s34, s42
	s_addc_u32 s39, s35, 0
	s_sub_u32 s40, s36, 0x4000
	s_subb_u32 s41, s37, 0
	s_sub_u32 s42, s38, 0x100
	s_subb_u32 s43, s39, 0
	s_add_i32 m0, s22, 0x4000
	s_nop 0
	global_load_lds_dwordx4 v145, s[40:41]
	s_add_i32 m0, s22, 0x4400
	s_nop 0
	global_load_lds_dwordx4 v149, s[40:41]
	s_add_i32 m0, s22, 0x6000
	s_nop 0
	global_load_lds_dwordx4 v148, s[42:43]
	s_add_i32 m0, s22, 0x6400
	s_nop 0
	global_load_lds_dwordx4 v147, s[42:43]
	v_bitop3_b32 v2, v54, v3, 7 bitop3:0x78
	v_lshlrev_b32_e32 v116, 4, v2
	v_bitop3_b32 v6, v54, v46, 2 bitop3:0x36
	v_lshlrev_b32_e32 v117, 4, v6
	v_bitop3_b32 v42, v54, v46, 4 bitop3:0x36
	v_bitop3_b32 v46, v54, v46, 6 bitop3:0x36
	v_lshlrev_b32_e32 v118, 4, v42
	v_lshlrev_b32_e32 v119, 4, v46
	v_bitop3_b32 v10, v54, v50, 2 bitop3:0x36
	v_lshlrev_b32_e32 v112, 4, v10
	v_bitop3_b32 v55, v54, v50, 4 bitop3:0x36
	v_bitop3_b32 v50, v54, v50, 6 bitop3:0x36
	v_lshlrev_b32_e32 v111, 4, v55
	v_lshlrev_b32_e32 v113, 4, v50
	v_mov_b32_e32 v2, 0
	v_mov_b32_e32 v3, 0
	v_mov_b32_e32 v4, 0
	v_mov_b32_e32 v5, 0
	v_mov_b32_e32 v6, 0
	v_mov_b32_e32 v7, 0
	v_mov_b32_e32 v8, 0
	v_mov_b32_e32 v9, 0
	v_mov_b32_e32 v10, 0
	v_mov_b32_e32 v11, 0
	v_mov_b32_e32 v12, 0
	v_mov_b32_e32 v13, 0
	v_mov_b32_e32 v14, 0
	v_mov_b32_e32 v15, 0
	v_mov_b32_e32 v16, 0
	v_mov_b32_e32 v17, 0
	v_mov_b32_e32 v18, 0
	v_mov_b32_e32 v19, 0
	v_mov_b32_e32 v20, 0
	v_mov_b32_e32 v21, 0
	v_mov_b32_e32 v22, 0
	v_mov_b32_e32 v23, 0
	v_mov_b32_e32 v24, 0
	v_mov_b32_e32 v25, 0
	v_mov_b32_e32 v26, 0
	v_mov_b32_e32 v27, 0
	v_mov_b32_e32 v28, 0
	v_mov_b32_e32 v29, 0
	v_mov_b32_e32 v30, 0
	v_mov_b32_e32 v31, 0
	v_mov_b32_e32 v32, 0
	v_mov_b32_e32 v33, 0
	v_mov_b32_e32 v34, 0
	v_mov_b32_e32 v35, 0
	v_mov_b32_e32 v36, 0
	v_mov_b32_e32 v37, 0
	v_mov_b32_e32 v38, 0
	v_mov_b32_e32 v39, 0
	v_mov_b32_e32 v40, 0
	v_mov_b32_e32 v41, 0
	v_mov_b32_e32 v42, 0
	v_mov_b32_e32 v43, 0
	v_mov_b32_e32 v44, 0
	v_mov_b32_e32 v45, 0
	v_mov_b32_e32 v46, 0
	v_mov_b32_e32 v47, 0
	v_mov_b32_e32 v48, 0
	v_mov_b32_e32 v49, 0
	v_mov_b32_e32 v114, 0
	s_mov_b32 s23, 0
	s_mov_b32 s9, 0
	s_mov_b32 s8, 0x46000000
	s_sub_u32 s36, s36, 0x2000
	s_subb_u32 s37, s37, 0
	s_sub_u32 s38, s38, 0x80
	s_subb_u32 s39, s39, 0
	s_mov_b32 s44, 0xff800000
	s_mov_b32 s45, 0x3c800000
